# grid barrier after the in-proj: non-last workgroups run the attention phase's pre-unit weight-conversion tiles before spinning on the release (split arrive/wait)
# baseline (speedup 1.0000x reference)
.LBB0_247:
	s_or_b64 exec, exec, s[8:9]
	v_cvt_f32_u32_e32 v6, v4
	s_waitcnt vmcnt(0)
	v_readfirstlane_b32 s2, v5
	v_sub_u32_e32 v5, 0, v4
	v_rcp_iflag_f32_e32 v6, v6
	v_add_u32_e32 v7, s2, v3
	v_mul_f32_e32 v6, 0x4f7ffffe, v6
	v_cvt_u32_f32_e32 v6, v6
	v_mul_lo_u32 v3, v5, v6
	v_mul_hi_u32 v3, v6, v3
	v_add_u32_e32 v3, v6, v3
	v_mul_hi_u32 v3, v7, v3
	v_mul_lo_u32 v5, v3, v4
	v_sub_u32_e32 v5, v7, v5
	v_add_u32_e32 v6, 1, v3
	v_cmp_ge_u32_e32 vcc, v5, v4
	s_nop 1
	v_cndmask_b32_e32 v3, v3, v6, vcc
	v_sub_u32_e32 v6, v5, v4
	v_cndmask_b32_e32 v5, v5, v6, vcc
	v_add_u32_e32 v6, 1, v3
	v_cmp_ge_u32_e32 vcc, v5, v4
	v_add_u32_e32 v5, 1, v7
	s_nop 0
	v_cndmask_b32_e32 v3, v3, v6, vcc
	v_mul_lo_u32 v6, v4, v3
	v_add_u32_e32 v4, v6, v4
	s_mov_b32 s99, 0
	v_cmp_ne_u32_e32 vcc, v5, v4
	s_and_saveexec_b64 s[2:3], vcc
	s_xor_b64 s[6:7], exec, s[2:3]
	s_cbranch_execz .LBB0_261
	v_readfirstlane_b32 s98, v3
	s_mov_b32 s99, 1

.LBB0_291:
	s_mov_b64 s[0:1], exec
	v_readlane_b32 s2, v253, 6
	v_readlane_b32 s3, v253, 7
	s_and_b64 s[2:3], s[0:1], s[2:3]
	s_mov_b64 exec, s[2:3]
	s_cbranch_execz .Ldw_done
	s_cmp_eq_u32 s99, 0
	s_cbranch_scc1 .Ldw_done
	s_mov_b32 s99, 0
	s_lshl_b32 s2, s96, 8
	v_readlane_b32 s4, v253, 2
	v_readlane_b32 s5, v253, 3
	s_nop 1
	s_add_u32 s4, s4, s2
	s_addc_u32 s5, s5, 0
	v_mov_b32_e32 v241, s98
	s_waitcnt lgkmcnt(0)
	v_mov_b32_e32 v240, 0x2000
	global_load_dword v240, v240, s[4:5] offset:1024 sc1
	s_add_u32 s62, s4, 0x2400
	s_addc_u32 s63, s5, 0
	s_waitcnt vmcnt(0)
	v_cmp_eq_u32_e32 vcc, v240, v241
	s_and_saveexec_b64 s[8:9], vcc
	s_cbranch_execz .Ldw_260
	s_add_u32 s60, s74, 0x4200
	s_addc_u32 s61, s75, 0
	s_mov_b32 s2, 1
	s_mov_b64 s[76:77], 0
	v_mov_b32_e32 v240, 0
	s_branch .Ldw_251
.Ldw_250:
	s_and_b64 s[80:81], exec, s[80:81]
	s_or_b64 s[76:77], s[80:81], s[76:77]
	s_andn2_b64 s[78:79], s[78:79], exec
	s_and_b64 s[80:81], s[82:83], exec
	s_or_b64 s[78:79], s[78:79], s[80:81]
	s_andn2_b64 exec, exec, s[76:77]
	s_cbranch_execz .Ldw_257
.Ldw_251:
	s_and_b32 s3, s2, 0xff
	s_mov_b64 s[80:81], -1
	s_cmp_lg_u32 s3, 0
	s_mov_b64 s[86:87], -1
	s_sleep 1
	s_cbranch_scc1 .Ldw_254
	global_load_dword v242, v240, s[60:61] sc1
	s_waitcnt vmcnt(0)
	v_cmp_eq_u32_e32 vcc, 0, v242
	s_cbranch_vccnz .Ldw_256
	s_mov_b64 s[86:87], 0
	s_mov_b64 s[82:83], -1

.Ldw_255:
	global_load_dword v242, v240, s[62:63] sc1
	s_add_i32 s2, s2, 1
	s_mov_b64 s[82:83], -1
	s_waitcnt vmcnt(0)
	v_cmp_ne_u32_e32 vcc, v242, v241
	s_orn2_b64 s[80:81], vcc, exec
	s_branch .Ldw_250
.Ldw_256:
	s_cmp_lt_u32 s2, 0x40001
	s_mov_b64 s[82:83], 0
	s_cselect_b64 s[86:87], -1, 0
	s_and_b64 vcc, exec, s[86:87]
	s_cbranch_vccz .Ldw_250
	s_branch .Ldw_255
.Ldw_257:
	s_or_b64 exec, exec, s[76:77]
	s_xor_b64 s[2:3], s[78:79], -1
	s_and_saveexec_b64 s[62:63], s[2:3]
	s_xor_b64 s[62:63], exec, s[62:63]
	s_cbranch_execz .Ldw_260
	s_mov_b64 s[62:63], exec
	v_mbcnt_lo_u32_b32 v240, s62, 0
	v_mbcnt_hi_u32_b32 v240, s63, v240
	v_cmp_eq_u32_e32 vcc, 0, v240
	s_and_b64 s[2:3], exec, vcc
	s_mov_b64 exec, s[2:3]
	s_cbranch_execz .Ldw_260
	s_bcnt1_i32_b64 s2, s[62:63]
	v_mov_b32_e32 v240, 0
	v_mov_b32_e32 v241, s2
	global_atomic_add v240, v241, s[60:61]

.Ldw_done:
	s_mov_b64 exec, s[0:1]
	s_barrier
	v_writelane_b32 v253, s36, 35
	s_mov_b32 s95, s92
	s_mov_b32 s88, s97
	v_writelane_b32 v253, s37, 36
	v_writelane_b32 v253, s40, 33
	s_cmpk_gt_i32 s97, 0xff
	s_nop 0
	v_writelane_b32 v253, s41, 34
	v_writelane_b32 v253, s93, 45
	s_cbranch_scc1 .LBB0_416
	v_mbcnt_lo_u32_b32 v2, -1, 0
	v_mbcnt_hi_u32_b32 v2, -1, v2
	v_and_b32_e32 v4, 64, v2
	v_xor_b32_e32 v3, 32, v2
	v_add_u32_e32 v4, 64, v4
	v_cmp_lt_i32_e32 vcc, v3, v4
	v_lshrrev_b32_e32 v4, 5, v218
	v_mov_b32_e32 v127, 0
	v_cndmask_b32_e32 v2, v2, v3, vcc
	s_lshl_b32 s2, s95, 1
	v_lshlrev_b32_e32 v126, 4, v4
	v_lshlrev_b32_e32 v129, 2, v2
	s_and_b32 s27, s2, 2
	v_lshl_add_u64 v[2:3], s[74:75], 0, v[126:127]
	s_mov_b64 s[2:3], 0x10000000
	v_lshl_add_u64 v[130:131], v[2:3], 0, s[2:3]
	v_and_b32_e32 v3, 7, v0
	v_lshlrev_b32_e32 v2, 4, v3
	v_add_u32_e32 v6, 0, v2
	s_movk_i32 s2, 0x1030
	v_mad_u32_u24 v7, v3, s2, v6
	v_mov_b32_e32 v3, v127
	v_lshl_add_u64 v[2:3], s[74:75], 0, v[2:3]
	s_mov_b64 s[2:3], 0x11000000
	v_lshl_add_u64 v[132:133], v[2:3], 0, s[2:3]
	v_lshrrev_b32_e32 v2, 2, v0
	v_and_b32_e32 v135, 0x7e, v2
	v_or_b32_e32 v2, 1, v2
	v_mul_u32_u24_e32 v9, 0x90, v2
	v_or_b32_e32 v2, 0x200, v0
	v_lshrrev_b32_e32 v3, 2, v2
	v_and_b32_e32 v202, 0xfe, v3
	v_or_b32_e32 v3, 1, v3
	v_mul_u32_u24_e32 v12, 0x90, v3
	v_lshrrev_b16_e32 v3, 3, v0
	v_mul_u32_u24_e32 v3, 0x147b, v3
	v_lshrrev_b32_e32 v3, 17, v3
	v_mul_lo_u16_e32 v14, 0xc8, v3
	v_sub_u16_e32 v14, v0, v14
	v_add_u16_e32 v14, v14, v3
	v_subrev_u16_e32 v3, 40, v14
	s_movk_i32 s20, 0x80
	v_mul_hi_u32_u24_e32 v204, 0x51eb86, v2
	v_cmp_gt_u16_e64 s[40:41], s20, v3
	v_mul_u32_u24_e32 v3, 0x320, v204
	v_sub_u32_e32 v3, v2, v3
	v_lshrrev_b16_e32 v15, 3, v3
	v_mul_u32_u24_e32 v15, 0x147b, v15
	v_lshrrev_b32_e32 v15, 17, v15
	v_mul_lo_u16_e32 v16, 0xc8, v15
	s_add_i32 s22, 0, 0x11200
	v_sub_u16_e32 v3, v3, v16
	v_mul_hi_u32_u24_e32 v206, 0x51eb86, v173
	v_add_u16_e32 v15, v3, v15
	v_lshl_add_u32 v205, v2, 2, s22
	v_mul_u32_u24_e32 v2, 0x320, v206
	v_subrev_u16_e32 v3, 40, v15
	v_sub_u32_e32 v2, v173, v2
	v_cmp_gt_u16_e64 s[58:59], s20, v3
	v_lshrrev_b16_e32 v3, 3, v2
	v_mul_u32_u24_e32 v3, 0x147b, v3
	v_lshrrev_b32_e32 v3, 17, v3
	v_mul_lo_u16_e32 v16, 0xc8, v3
	v_sub_u16_e32 v2, v2, v16
	v_add_u16_e32 v16, v2, v3
	v_readlane_b32 s0, v253, 30
	v_subrev_u16_e32 v2, 40, v16
	s_lshr_b32 s26, s0, 7
	v_cmp_gt_u16_e64 s[0:1], s20, v2
	v_or_b32_e32 v2, 0x600, v0
	v_mul_hi_u32_u24_e32 v208, 0x51eb86, v2
	v_mul_u32_u24_e32 v3, 0x320, v208
	v_sub_u32_e32 v3, v2, v3
	v_lshrrev_b16_e32 v17, 3, v3
	v_mul_u32_u24_e32 v17, 0x147b, v17
	v_lshrrev_b32_e32 v17, 17, v17
	v_mul_lo_u16_e32 v18, 0xc8, v17
	v_sub_u16_e32 v3, v3, v18
	v_mul_hi_u32_u24_e32 v210, 0x51eb86, v171
	v_add_u16_e32 v17, v3, v17
	v_lshl_add_u32 v209, v2, 2, s22
	v_mul_u32_u24_e32 v2, 0x320, v210
	v_subrev_u16_e32 v3, 40, v17
	v_sub_u32_e32 v2, v171, v2
	v_cmp_gt_u16_e64 s[56:57], s20, v3
	v_lshrrev_b16_e32 v3, 3, v2
	v_mul_u32_u24_e32 v3, 0x147b, v3
	v_lshrrev_b32_e32 v3, 17, v3
	v_mul_lo_u16_e32 v18, 0xc8, v3
	v_sub_u16_e32 v2, v2, v18
	v_add_u16_e32 v18, v2, v3
	v_subrev_u16_e32 v2, 40, v18
	s_movk_i32 s3, 0x280
	v_cmp_gt_u16_e64 s[54:55], s20, v2
	v_cmp_gt_u32_e64 s[64:65], s3, v0
	s_lshl_b32 s3, s26, 2
	v_lshlrev_b32_e32 v134, 2, v4
	v_bfi_b32 v2, v0, 31, 3
	s_movk_i32 s2, 0xc8
	v_or_b32_e32 v19, 0xa00, v0
	v_bitop3_b32 v3, s3, v0, 3 bitop3:0xf2
	v_sub_u32_e32 v2, v134, v2
	v_mad_u64_u32 v[2:3], s[2:3], v3, s2, v[2:3]
	v_mul_hi_u32_u24_e32 v214, 0x51eb86, v19
	s_lshl_b32 s30, s27, 5
	v_mul_u32_u24_e32 v3, 0x320, v214
	s_or_b32 s31, s30, 32
	v_sub_u32_e32 v3, v19, v3
	v_lshlrev_b32_e32 v5, 3, v4
	s_bitcmp1_b32 s95, 0
	v_lshrrev_b16_e32 v4, 3, v3
	v_add_u32_e32 v213, 0, v126
	s_cselect_b64 s[62:63], -1, 0
	v_sub_u16_e32 v126, 0xa7, v14
	s_getpc_b64 s[2:3]
	s_add_u32 s2, s2, _ZL9T5_BUCKET@rel32@lo+4
	s_addc_u32 s3, s3, _ZL9T5_BUCKET@rel32@hi+12
	v_mul_u32_u24_e32 v4, 0x147b, v4
	v_lshl_add_u64 v[136:137], s[2:3], 0, v[126:127]
	v_sub_u16_e32 v126, 0xa7, v15
	v_lshrrev_b32_e32 v4, 17, v4
	v_lshl_add_u64 v[138:139], s[2:3], 0, v[126:127]
	v_sub_u16_e32 v126, 0xa7, v16
	v_mul_lo_u16_e32 v14, 0xc8, v4
	v_lshl_add_u64 v[140:141], s[2:3], 0, v[126:127]
	v_sub_u16_e32 v126, 0xa7, v17
	v_sub_u16_e32 v3, v3, v14
	v_lshl_add_u64 v[142:143], s[2:3], 0, v[126:127]
	v_sub_u16_e32 v126, 0xa7, v18
	v_add_u16_e32 v3, v3, v4
	v_mul_hi_u32_u24_e32 v216, 0x51eb86, v1
	v_lshl_add_u64 v[144:145], s[2:3], 0, v[126:127]
	v_subrev_u16_e32 v4, 40, v3
	v_sub_u16_e32 v126, 0xa7, v3
	v_mul_u32_u24_e32 v3, 0x320, v216
	v_sub_u32_e32 v3, v1, v3
	v_cmp_gt_u16_e64 s[4:5], s20, v4
	v_lshrrev_b16_e32 v4, 3, v3
	v_mul_u32_u24_e32 v4, 0x147b, v4
	v_lshrrev_b32_e32 v4, 17, v4
	v_mul_lo_u16_e32 v14, 0xc8, v4
	v_sub_u16_e32 v3, v3, v14
	v_and_b32_e32 v128, 31, v0
	v_lshl_add_u32 v2, v2, 2, s22
	v_add_u16_e32 v3, v3, v4
	v_mul_u32_u24_e32 v8, 0x90, v135
	v_lshlrev_b32_e32 v10, 1, v135
	v_mul_u32_u24_e32 v11, 0x90, v202
	v_lshlrev_b32_e32 v13, 1, v202
	v_add_u32_e32 v212, 0x9c, v2
	v_mul_u32_u24_e32 v2, 0x208, v128
	v_lshl_add_u64 v[146:147], s[2:3], 0, v[126:127]
	v_subrev_u16_e32 v4, 40, v3
	v_sub_u16_e32 v126, 0xa7, v3
	s_mov_b32 s61, 0
	s_movk_i32 s34, 0x7e
	s_movk_i32 s35, 0x90
	v_lshl_add_u32 v203, v0, 2, s22
	v_lshl_add_u32 v207, v173, 2, s22
	v_lshl_add_u32 v211, v171, 2, s22
	v_cmp_gt_u32_e64 s[96:97], s20, v0
	v_writelane_b32 v253, s4, 31
	v_lshl_add_u32 v215, v19, 2, s22
	v_cmp_gt_u16_e64 s[20:21], s20, v4
	v_lshl_add_u64 v[148:149], s[2:3], 0, v[126:127]
	v_lshl_add_u32 v1, v1, 2, s22
	v_add3_u32 v217, 0, v5, v2
	v_add_u32_e32 v219, v6, v8
	v_add_u32_e32 v220, v6, v9
	s_mov_b32 s36, 0xffff
	v_add_u32_e32 v221, v7, v10
	s_mov_b32 s37, 0xffff0000
	v_add_u32_e32 v222, v6, v11
	v_add_u32_e32 v223, v6, v12
	v_add_u32_e32 v224, v7, v13
	s_mov_b32 s66, 0x3fb8aa3b
	s_movk_i32 s67, 0x76
	s_movk_i32 s84, 0x75
	s_movk_i32 s85, 0x74
	s_movk_i32 s86, 0x6e
	s_movk_i32 s87, 0x6d
	s_movk_i32 s89, 0x6c
	s_movk_i32 s91, 0x66
	s_movk_i32 s92, 0x65
	s_movk_i32 s93, 0x64
	s_mov_b32 s94, s88
	v_writelane_b32 v253, s5, 32
	s_branch .LBB0_294

	.amdhsa_kernel _Z6mk_fwd4Args
		.amdhsa_group_segment_fixed_size 0
		.amdhsa_private_segment_fixed_size 0
		.amdhsa_kernarg_size 424
		.amdhsa_user_sgpr_count 2
		.amdhsa_user_sgpr_dispatch_ptr 0
		.amdhsa_user_sgpr_queue_ptr 0
		.amdhsa_user_sgpr_kernarg_segment_ptr 1
		.amdhsa_user_sgpr_dispatch_id 0
		.amdhsa_user_sgpr_kernarg_preload_length 0
		.amdhsa_user_sgpr_kernarg_preload_offset 0
		.amdhsa_user_sgpr_private_segment_size 0
		.amdhsa_uses_dynamic_stack 0
		.amdhsa_enable_private_segment 0
		.amdhsa_system_sgpr_workgroup_id_x 1
		.amdhsa_system_sgpr_workgroup_id_y 0
		.amdhsa_system_sgpr_workgroup_id_z 0
		.amdhsa_system_sgpr_workgroup_info 0
		.amdhsa_system_vgpr_workitem_id 0
		.amdhsa_next_free_vgpr 254
		.amdhsa_next_free_sgpr 102
		.amdhsa_accum_offset 256
		.amdhsa_reserve_vcc 1
		.amdhsa_float_round_mode_32 0
		.amdhsa_float_round_mode_16_64 0
		.amdhsa_float_denorm_mode_32 3
		.amdhsa_float_denorm_mode_16_64 3
		.amdhsa_dx10_clamp 1
		.amdhsa_ieee_mode 1
		.amdhsa_fp16_overflow 0
		.amdhsa_tg_split 0
		.amdhsa_exception_fp_ieee_invalid_op 0
		.amdhsa_exception_fp_denorm_src 0
		.amdhsa_exception_fp_ieee_div_zero 0
		.amdhsa_exception_fp_ieee_overflow 0
		.amdhsa_exception_fp_ieee_underflow 0
		.amdhsa_exception_fp_ieee_inexact 0
		.amdhsa_exception_int_div_zero 0
	.end_amdhsa_kernel

amdhsa.kernels:
  - .agpr_count:     0
    .args:
      - .offset:         0
        .size:           168
        .value_kind:     by_value
      - .offset:         168
        .size:           4
        .value_kind:     hidden_block_count_x
      - .offset:         172
        .size:           4
        .value_kind:     hidden_block_count_y
      - .offset:         176
        .size:           4
        .value_kind:     hidden_block_count_z
      - .offset:         180
        .size:           2
        .value_kind:     hidden_group_size_x
      - .offset:         182
        .size:           2
        .value_kind:     hidden_group_size_y
      - .offset:         184
        .size:           2
        .value_kind:     hidden_group_size_z
      - .offset:         186
        .size:           2
        .value_kind:     hidden_remainder_x
      - .offset:         188
        .size:           2
        .value_kind:     hidden_remainder_y
      - .offset:         190
        .size:           2
        .value_kind:     hidden_remainder_z
      - .offset:         208
        .size:           8
        .value_kind:     hidden_global_offset_x
      - .offset:         216
        .size:           8
        .value_kind:     hidden_global_offset_y
      - .offset:         224
        .size:           8
        .value_kind:     hidden_global_offset_z
      - .offset:         232
        .size:           2
        .value_kind:     hidden_grid_dims
      - .offset:         288
        .size:           4
        .value_kind:     hidden_dynamic_lds_size
    .group_segment_fixed_size: 0
    .kernarg_segment_align: 8
    .kernarg_segment_size: 424
    .language:       OpenCL C
    .language_version:
      - 2
      - 0
    .max_flat_workgroup_size: 512
    .name:           _Z6mk_fwd4Args
    .private_segment_fixed_size: 0
    .sgpr_count:     108
    .sgpr_spill_count: 82
    .symbol:         _Z6mk_fwd4Args.kd
    .uniform_work_group_size: 1
    .uses_dynamic_stack: false
    .vgpr_count:     254
    .vgpr_spill_count: 0
    .wavefront_size: 64
